# v11 + nt on the BRANCH / WOUT / MOE2 epilogue dwordx4 stores
# baseline (speedup 1.0000x reference)
.LBB0_1116:
	v_mbcnt_lo_u32_b32 v252, -1, 0
	v_mbcnt_hi_u32_b32 v252, -1, v252
	v_bfe_u32 v252, v252, 4, 1
	v_mul_u32_u24_e32 v252, 0x78, v252
	v_mov_b32_e32 v253, 0
	v_ashrrev_i32_e32 v211, 31, v210
	v_ashrrev_i32_e32 v213, 31, v212
	v_lshl_add_u64 v[2:3], v[210:211], 1, s[24:25]
	v_lshlrev_b64 v[4:5], 12, v[212:213]
	v_lshl_add_u64 v[4:5], v[2:3], 0, v[4:5]
	global_load_dwordx4 v[60:63], v[4:5], off
	global_load_dwordx4 v[214:217], v[4:5], off offset:256
	v_or_b32_e32 v58, 16, v212
	v_or_b32_e32 v56, 32, v212
	v_or_b32_e32 v54, 48, v212
	v_add_u32_e32 v52, 0x80, v212
	v_add_u32_e32 v50, 0x90, v212
	v_add_u32_e32 v48, 0xa0, v212
	v_add_u32_e32 v46, 0xb0, v212
	v_ashrrev_i32_e32 v59, 31, v58
	v_ashrrev_i32_e32 v57, 31, v56
	v_ashrrev_i32_e32 v55, 31, v54
	v_ashrrev_i32_e32 v53, 31, v52
	v_ashrrev_i32_e32 v51, 31, v50
	v_ashrrev_i32_e32 v49, 31, v48
	v_ashrrev_i32_e32 v47, 31, v46
	v_lshlrev_b64 v[212:213], 11, v[212:213]
	v_lshlrev_b64 v[4:5], 12, v[58:59]
	v_lshlrev_b64 v[6:7], 12, v[56:57]
	v_lshlrev_b64 v[8:9], 12, v[54:55]
	v_lshlrev_b64 v[10:11], 12, v[52:53]
	v_lshlrev_b64 v[12:13], 12, v[50:51]
	v_lshlrev_b64 v[14:15], 12, v[48:49]
	v_lshlrev_b64 v[16:17], 12, v[46:47]
	v_lshl_add_u64 v[18:19], s[26:27], 0, v[212:213]
	v_lshl_add_u64 v[4:5], v[2:3], 0, v[4:5]
	v_lshl_add_u64 v[6:7], v[2:3], 0, v[6:7]
	v_lshl_add_u64 v[8:9], v[2:3], 0, v[8:9]
	v_lshl_add_u64 v[10:11], v[2:3], 0, v[10:11]
	v_lshl_add_u64 v[12:13], v[2:3], 0, v[12:13]
	v_lshl_add_u64 v[236:237], v[2:3], 0, v[14:15]
	v_lshl_add_u64 v[2:3], v[2:3], 0, v[16:17]
	v_lshl_add_u64 v[238:239], v[18:19], 0, v[210:211]
	global_load_dwordx4 v[218:221], v[4:5], off
	global_load_dwordx4 v[228:231], v[4:5], off offset:256
	global_load_dwordx4 v[232:235], v[6:7], off
	global_load_dwordx4 v[42:45], v[6:7], off offset:256
	global_load_dwordx4 v[38:41], v[8:9], off
	global_load_dwordx4 v[34:37], v[8:9], off offset:256
	global_load_dwordx4 v[30:33], v[10:11], off
	global_load_dwordx4 v[26:29], v[10:11], off offset:256
	global_load_dwordx4 v[22:25], v[12:13], off
	global_load_dwordx4 v[18:21], v[12:13], off offset:256
	global_load_dwordx4 v[14:17], v[236:237], off
	s_nop 0
	global_load_dwordx4 v[10:13], v[236:237], off offset:256
	global_load_dwordx4 v[6:9], v[2:3], off
	s_nop 0
	global_load_dwordx4 v[2:5], v[2:3], off offset:256
	v_mov_b32_e32 v64, v199
	v_mov_b32_e32 v65, v199
	v_lshlrev_b64 v[58:59], 11, v[58:59]
	v_lshlrev_b64 v[56:57], 11, v[56:57]
	s_waitcnt vmcnt(0)
	v_lshlrev_b32_e32 v201, 16, v60
	v_and_b32_e32 v60, 0xffff0000, v60
	v_lshlrev_b32_e32 v205, 16, v62
	v_and_b32_e32 v62, 0xffff0000, v62
	v_lshlrev_b32_e32 v236, 16, v63
	v_mul_f32_e32 v190, v190, v201
	v_mul_f32_e32 v60, v191, v60
	v_mul_f32_e32 v186, v186, v205
	v_mul_f32_e32 v62, v187, v62
	v_mul_f32_e32 v187, v188, v236
	v_mul_f32_e32 v188, 0x3c800000, v190
	v_mul_f32_e32 v60, 0x3c800000, v60
	v_mul_f32_e32 v186, 0x3c800000, v186
	v_mul_f32_e32 v62, 0x3c800000, v62
	v_med3_f32 v188, v188, s73, v227
	v_med3_f32 v60, v60, s73, v227
	v_med3_f32 v186, v186, s73, v227
	v_med3_f32 v62, v62, s73, v227
	v_lshlrev_b32_e32 v203, 16, v61
	v_and_b32_e32 v61, 0xffff0000, v61
	v_and_b32_e32 v63, 0xffff0000, v63
	v_cvt_pk_fp8_f32 v64, v188, v60
	v_cvt_pk_fp8_f32 v65, v186, v62
	v_mul_f32_e32 v191, v192, v203
	v_mul_f32_e32 v61, v193, v61
	v_mul_f32_e32 v63, v189, v63
	v_mul_f32_e32 v189, 0x3c800000, v191
	v_mul_f32_e32 v61, 0x3c800000, v61
	v_mul_f32_e32 v187, 0x3c800000, v187
	v_mul_f32_e32 v63, 0x3c800000, v63
	v_med3_f32 v189, v189, s73, v227
	v_med3_f32 v61, v61, s73, v227
	v_med3_f32 v60, v187, s73, v227
	v_med3_f32 v62, v63, s73, v227
	v_cvt_pk_fp8_f32 v64, v189, v61 op_sel:[0,0,1]
	v_cvt_pk_fp8_f32 v65, v60, v62 op_sel:[0,0,1]
	v_lshlrev_b32_e32 v237, 16, v214
	v_and_b32_e32 v214, 0xffff0000, v214
	v_lshlrev_b32_e32 v60, 16, v215
	v_mul_f32_e32 v61, v182, v237
	v_mul_f32_e32 v62, v183, v214
	v_mov_b32_e32 v240, v64
	v_mov_b32_e32 v241, v65
	v_mul_f32_e32 v60, v184, v60
	v_lshlrev_b32_e32 v64, 16, v216
	v_and_b32_e32 v65, 0xffff0000, v216
	v_mul_f32_e32 v64, v178, v64
	v_mul_f32_e32 v65, v179, v65
	v_lshlrev_b32_e32 v178, 16, v217
	v_mul_f32_e32 v61, 0x3c800000, v61
	v_mul_f32_e32 v62, 0x3c800000, v62
	v_mul_f32_e32 v60, 0x3c800000, v60
	v_mul_f32_e32 v178, v180, v178
	v_mul_f32_e32 v64, 0x3c800000, v64
	v_mul_f32_e32 v65, 0x3c800000, v65
	v_med3_f32 v61, v61, s73, v227
	v_med3_f32 v62, v62, s73, v227
	v_med3_f32 v180, v60, s73, v227
	v_mov_b32_e32 v60, v199
	v_and_b32_e32 v63, 0xffff0000, v215
	v_cvt_pk_fp8_f32 v60, v61, v62
	v_med3_f32 v62, v64, s73, v227
	v_med3_f32 v64, v65, s73, v227
	v_mov_b32_e32 v61, v199
	v_mul_f32_e32 v63, v185, v63
	v_and_b32_e32 v179, 0xffff0000, v217
	v_cvt_pk_fp8_f32 v61, v62, v64
	v_mul_f32_e32 v179, v181, v179
	v_mul_f32_e32 v63, 0x3c800000, v63
	v_mul_f32_e32 v178, 0x3c800000, v178
	v_mul_f32_e32 v179, 0x3c800000, v179
	v_med3_f32 v63, v63, s73, v227
	v_cvt_pk_fp8_f32 v60, v180, v63 op_sel:[0,0,1]
	v_med3_f32 v62, v178, s73, v227
	v_med3_f32 v63, v179, s73, v227
	v_cvt_pk_fp8_f32 v61, v62, v63 op_sel:[0,0,1]
	v_lshl_add_u64 v[62:63], s[8:9], 0, v[212:213]
	v_lshl_add_u64 v[62:63], v[62:63], 0, v[210:211]
	v_add_co_u32_e32 v62, vcc, s74, v62
	v_lshlrev_b32_e32 v64, 16, v220
	s_nop 0
	v_addc_co_u32_e32 v63, vcc, 0, v63, vcc
	v_mov_b32_e32 v242, v60
	v_mov_b32_e32 v243, v61
	v_lshl_add_u64 v[248:249], v[62:63], 0, v[252:253]
	s_nop 1
	v_permlane16_swap_b32_e32 v240, v242
	v_permlane16_swap_b32_e32 v241, v243
	global_store_dwordx4 v[248:249], v[240:243], off nt
	v_lshlrev_b32_e32 v60, 16, v218
	v_and_b32_e32 v61, 0xffff0000, v218
	v_mul_f32_e32 v60, v174, v60
	v_mul_f32_e32 v61, v175, v61
	v_and_b32_e32 v65, 0xffff0000, v220
	v_mul_f32_e32 v64, v170, v64
	v_mul_f32_e32 v65, v171, v65
	v_lshlrev_b32_e32 v170, 16, v221
	v_mul_f32_e32 v60, 0x3c800000, v60
	v_mul_f32_e32 v61, 0x3c800000, v61
	v_mul_f32_e32 v170, v172, v170
	v_mul_f32_e32 v64, 0x3c800000, v64
	v_mul_f32_e32 v65, 0x3c800000, v65
	v_med3_f32 v172, v60, s73, v227
	v_med3_f32 v61, v61, s73, v227
	v_mov_b32_e32 v60, v199
	v_lshlrev_b32_e32 v62, 16, v219
	v_and_b32_e32 v63, 0xffff0000, v219
	v_cvt_pk_fp8_f32 v60, v172, v61
	v_med3_f32 v64, v64, s73, v227
	v_med3_f32 v65, v65, s73, v227
	v_mov_b32_e32 v61, v199
	v_mul_f32_e32 v62, v176, v62
	v_mul_f32_e32 v63, v177, v63
	v_and_b32_e32 v171, 0xffff0000, v221
	v_cvt_pk_fp8_f32 v61, v64, v65
	v_mul_f32_e32 v171, v173, v171
	v_mul_f32_e32 v62, 0x3c800000, v62
	v_mul_f32_e32 v63, 0x3c800000, v63
	v_mul_f32_e32 v170, 0x3c800000, v170
	v_mul_f32_e32 v171, 0x3c800000, v171
	v_med3_f32 v62, v62, s73, v227
	v_med3_f32 v63, v63, s73, v227
	v_cvt_pk_fp8_f32 v60, v62, v63 op_sel:[0,0,1]
	v_med3_f32 v62, v170, s73, v227
	v_med3_f32 v63, v171, s73, v227
	v_cvt_pk_fp8_f32 v61, v62, v63 op_sel:[0,0,1]
	v_lshl_add_u64 v[62:63], s[26:27], 0, v[58:59]
	v_lshl_add_u64 v[62:63], v[62:63], 0, v[210:211]
	v_lshlrev_b32_e32 v64, 16, v230
	v_mov_b32_e32 v244, v60
	v_mov_b32_e32 v245, v61
	v_lshlrev_b32_e32 v60, 16, v228
	v_and_b32_e32 v61, 0xffff0000, v228
	v_mul_f32_e32 v60, v166, v60
	v_mul_f32_e32 v61, v167, v61
	v_and_b32_e32 v65, 0xffff0000, v230
	v_mul_f32_e32 v64, v162, v64
	v_mul_f32_e32 v65, v163, v65
	v_lshlrev_b32_e32 v162, 16, v231
	v_mul_f32_e32 v60, 0x3c800000, v60
	v_mul_f32_e32 v61, 0x3c800000, v61
	v_mul_f32_e32 v162, v164, v162
	v_mul_f32_e32 v64, 0x3c800000, v64
	v_mul_f32_e32 v65, 0x3c800000, v65
	v_med3_f32 v164, v60, s73, v227
	v_med3_f32 v61, v61, s73, v227
	v_mov_b32_e32 v60, v199
	v_lshlrev_b32_e32 v62, 16, v229
	v_and_b32_e32 v63, 0xffff0000, v229
	v_cvt_pk_fp8_f32 v60, v164, v61
	v_med3_f32 v64, v64, s73, v227
	v_med3_f32 v65, v65, s73, v227
	v_mov_b32_e32 v61, v199
	v_mul_f32_e32 v62, v168, v62
	v_mul_f32_e32 v63, v169, v63
	v_and_b32_e32 v163, 0xffff0000, v231
	v_cvt_pk_fp8_f32 v61, v64, v65
	v_mul_f32_e32 v163, v165, v163
	v_mul_f32_e32 v62, 0x3c800000, v62
	v_mul_f32_e32 v63, 0x3c800000, v63
	v_mul_f32_e32 v162, 0x3c800000, v162
	v_mul_f32_e32 v163, 0x3c800000, v163
	v_med3_f32 v62, v62, s73, v227
	v_med3_f32 v63, v63, s73, v227
	v_cvt_pk_fp8_f32 v60, v62, v63 op_sel:[0,0,1]
	v_med3_f32 v62, v162, s73, v227
	v_med3_f32 v63, v163, s73, v227
	v_cvt_pk_fp8_f32 v61, v62, v63 op_sel:[0,0,1]
	v_lshl_add_u64 v[58:59], s[8:9], 0, v[58:59]
	v_lshl_add_u64 v[58:59], v[58:59], 0, v[210:211]
	v_add_co_u32_e32 v58, vcc, s74, v58
	v_lshlrev_b32_e32 v62, 16, v234
	s_nop 0
	v_addc_co_u32_e32 v59, vcc, 0, v59, vcc
	v_mov_b32_e32 v246, v60
	v_mov_b32_e32 v247, v61
	v_lshl_add_u64 v[250:251], v[58:59], 0, v[252:253]
	s_nop 1
	v_permlane16_swap_b32_e32 v244, v246
	v_permlane16_swap_b32_e32 v245, v247
	global_store_dwordx4 v[250:251], v[244:247], off nt
	v_lshlrev_b32_e32 v58, 16, v232
	v_and_b32_e32 v59, 0xffff0000, v232
	v_mul_f32_e32 v58, v158, v58
	v_mul_f32_e32 v59, v159, v59
	v_and_b32_e32 v63, 0xffff0000, v234
	v_mul_f32_e32 v62, v154, v62
	v_mul_f32_e32 v63, v155, v63
	v_mul_f32_e32 v58, 0x3c800000, v58
	v_mul_f32_e32 v59, 0x3c800000, v59
	v_mul_f32_e32 v62, 0x3c800000, v62
	v_mul_f32_e32 v63, 0x3c800000, v63
	v_med3_f32 v154, v58, s73, v227
	v_med3_f32 v59, v59, s73, v227
	v_mov_b32_e32 v58, v199
	v_lshlrev_b32_e32 v60, 16, v233
	v_and_b32_e32 v61, 0xffff0000, v233
	v_cvt_pk_fp8_f32 v58, v154, v59
	v_med3_f32 v62, v62, s73, v227
	v_med3_f32 v63, v63, s73, v227
	v_mov_b32_e32 v59, v199
	v_mul_f32_e32 v60, v160, v60
	v_mul_f32_e32 v61, v161, v61
	v_lshlrev_b32_e32 v64, 16, v235
	v_and_b32_e32 v65, 0xffff0000, v235
	v_cvt_pk_fp8_f32 v59, v62, v63
	v_mul_f32_e32 v64, v156, v64
	v_mul_f32_e32 v65, v157, v65
	v_mul_f32_e32 v60, 0x3c800000, v60
	v_mul_f32_e32 v61, 0x3c800000, v61
	v_mul_f32_e32 v64, 0x3c800000, v64
	v_mul_f32_e32 v65, 0x3c800000, v65
	v_med3_f32 v60, v60, s73, v227
	v_med3_f32 v61, v61, s73, v227
	v_cvt_pk_fp8_f32 v58, v60, v61 op_sel:[0,0,1]
	v_med3_f32 v60, v64, s73, v227
	v_med3_f32 v61, v65, s73, v227
	v_cvt_pk_fp8_f32 v59, v60, v61 op_sel:[0,0,1]
	v_lshl_add_u64 v[60:61], s[26:27], 0, v[56:57]
	v_lshl_add_u64 v[60:61], v[60:61], 0, v[210:211]
	v_mov_b32_e32 v240, v58
	v_mov_b32_e32 v241, v59
	v_lshlrev_b32_e32 v58, 16, v42
	v_and_b32_e32 v42, 0xffff0000, v42
	v_mul_f32_e32 v58, v150, v58
	v_mul_f32_e32 v42, v151, v42
	v_lshlrev_b32_e32 v59, 16, v43
	v_and_b32_e32 v43, 0xffff0000, v43
	v_lshlrev_b32_e32 v60, 16, v44
	v_and_b32_e32 v44, 0xffff0000, v44
	v_mul_f32_e32 v43, v153, v43
	v_mul_f32_e32 v60, v146, v60
	v_mul_f32_e32 v44, v147, v44
	v_mul_f32_e32 v58, 0x3c800000, v58
	v_mul_f32_e32 v42, 0x3c800000, v42
	v_mul_f32_e32 v43, 0x3c800000, v43
	v_mul_f32_e32 v60, 0x3c800000, v60
	v_mul_f32_e32 v44, 0x3c800000, v44
	v_med3_f32 v58, v58, s73, v227
	v_med3_f32 v62, v42, s73, v227
	v_mov_b32_e32 v42, v199
	v_med3_f32 v63, v43, s73, v227
	v_cvt_pk_fp8_f32 v42, v58, v62
	v_med3_f32 v58, v60, s73, v227
	v_med3_f32 v44, v44, s73, v227
	v_mov_b32_e32 v43, v199
	v_lshlrev_b32_e32 v61, 16, v45
	v_and_b32_e32 v45, 0xffff0000, v45
	v_cvt_pk_fp8_f32 v43, v58, v44
	v_mul_f32_e32 v59, v152, v59
	v_mul_f32_e32 v61, v148, v61
	v_mul_f32_e32 v45, v149, v45
	v_mul_f32_e32 v59, 0x3c800000, v59
	v_mul_f32_e32 v61, 0x3c800000, v61
	v_mul_f32_e32 v45, 0x3c800000, v45
	v_med3_f32 v59, v59, s73, v227
	v_med3_f32 v44, v61, s73, v227
	v_med3_f32 v45, v45, s73, v227
	v_cvt_pk_fp8_f32 v42, v59, v63 op_sel:[0,0,1]
	v_cvt_pk_fp8_f32 v43, v44, v45 op_sel:[0,0,1]
	v_lshl_add_u64 v[44:45], s[8:9], 0, v[56:57]
	v_lshl_add_u64 v[44:45], v[44:45], 0, v[210:211]
	v_add_co_u32_e32 v44, vcc, s74, v44
	s_nop 1
	v_addc_co_u32_e32 v45, vcc, 0, v45, vcc
	v_mov_b32_e32 v242, v42
	v_mov_b32_e32 v243, v43
	v_lshl_add_u64 v[248:249], v[44:45], 0, v[252:253]
	s_nop 1
	v_permlane16_swap_b32_e32 v240, v242
	v_permlane16_swap_b32_e32 v241, v243
	global_store_dwordx4 v[248:249], v[240:243], off nt
	v_lshlrev_b32_e32 v42, 16, v38
	v_and_b32_e32 v38, 0xffff0000, v38
	v_mul_f32_e32 v42, v142, v42
	v_mul_f32_e32 v38, v143, v38
	v_lshlrev_b32_e32 v43, 16, v39
	v_and_b32_e32 v39, 0xffff0000, v39
	v_lshlrev_b32_e32 v44, 16, v40
	v_and_b32_e32 v40, 0xffff0000, v40
	v_mul_f32_e32 v39, v145, v39
	v_mul_f32_e32 v44, v138, v44
	v_mul_f32_e32 v40, v139, v40
	v_mul_f32_e32 v42, 0x3c800000, v42
	v_mul_f32_e32 v38, 0x3c800000, v38
	v_mul_f32_e32 v39, 0x3c800000, v39
	v_mul_f32_e32 v44, 0x3c800000, v44
	v_mul_f32_e32 v40, 0x3c800000, v40
	v_med3_f32 v42, v42, s73, v227
	v_med3_f32 v56, v38, s73, v227
	v_mov_b32_e32 v38, v199
	v_med3_f32 v57, v39, s73, v227
	v_cvt_pk_fp8_f32 v38, v42, v56
	v_med3_f32 v42, v44, s73, v227
	v_med3_f32 v40, v40, s73, v227
	v_mov_b32_e32 v39, v199
	v_lshlrev_b32_e32 v45, 16, v41
	v_and_b32_e32 v41, 0xffff0000, v41
	v_cvt_pk_fp8_f32 v39, v42, v40
	v_mul_f32_e32 v43, v144, v43
	v_mul_f32_e32 v45, v140, v45
	v_mul_f32_e32 v41, v141, v41
	v_mul_f32_e32 v43, 0x3c800000, v43
	v_mul_f32_e32 v45, 0x3c800000, v45
	v_mul_f32_e32 v41, 0x3c800000, v41
	v_med3_f32 v43, v43, s73, v227
	v_med3_f32 v40, v45, s73, v227
	v_med3_f32 v41, v41, s73, v227
	v_cvt_pk_fp8_f32 v38, v43, v57 op_sel:[0,0,1]
	v_cvt_pk_fp8_f32 v39, v40, v41 op_sel:[0,0,1]
	v_lshlrev_b64 v[40:41], 11, v[54:55]
	v_lshl_add_u64 v[42:43], s[26:27], 0, v[40:41]
	v_lshl_add_u64 v[42:43], v[42:43], 0, v[210:211]
	v_mov_b32_e32 v244, v38
	v_mov_b32_e32 v245, v39
	v_lshlrev_b32_e32 v38, 16, v34
	v_and_b32_e32 v34, 0xffff0000, v34
	v_mul_f32_e32 v38, v134, v38
	v_mul_f32_e32 v34, v135, v34
	v_lshlrev_b32_e32 v39, 16, v35
	v_and_b32_e32 v35, 0xffff0000, v35
	v_lshlrev_b32_e32 v42, 16, v36
	v_and_b32_e32 v36, 0xffff0000, v36
	v_mul_f32_e32 v35, v137, v35
	v_mul_f32_e32 v42, v130, v42
	v_mul_f32_e32 v36, v131, v36
	v_mul_f32_e32 v38, 0x3c800000, v38
	v_mul_f32_e32 v34, 0x3c800000, v34
	v_mul_f32_e32 v35, 0x3c800000, v35
	v_mul_f32_e32 v42, 0x3c800000, v42
	v_mul_f32_e32 v36, 0x3c800000, v36
	v_med3_f32 v38, v38, s73, v227
	v_med3_f32 v44, v34, s73, v227
	v_mov_b32_e32 v34, v199
	v_med3_f32 v45, v35, s73, v227
	v_cvt_pk_fp8_f32 v34, v38, v44
	v_med3_f32 v38, v42, s73, v227
	v_med3_f32 v36, v36, s73, v227
	v_mov_b32_e32 v35, v199
	v_lshlrev_b32_e32 v43, 16, v37
	v_and_b32_e32 v37, 0xffff0000, v37
	v_cvt_pk_fp8_f32 v35, v38, v36
	v_mul_f32_e32 v39, v136, v39
	v_mul_f32_e32 v43, v132, v43
	v_mul_f32_e32 v37, v133, v37
	v_mul_f32_e32 v39, 0x3c800000, v39
	v_mul_f32_e32 v43, 0x3c800000, v43
	v_mul_f32_e32 v37, 0x3c800000, v37
	v_med3_f32 v39, v39, s73, v227
	v_med3_f32 v36, v43, s73, v227
	v_med3_f32 v37, v37, s73, v227
	v_cvt_pk_fp8_f32 v34, v39, v45 op_sel:[0,0,1]
	v_cvt_pk_fp8_f32 v35, v36, v37 op_sel:[0,0,1]
	v_lshl_add_u64 v[36:37], s[8:9], 0, v[40:41]
	v_lshl_add_u64 v[36:37], v[36:37], 0, v[210:211]
	v_add_co_u32_e32 v36, vcc, s74, v36
	s_nop 1
	v_addc_co_u32_e32 v37, vcc, 0, v37, vcc
	v_mov_b32_e32 v246, v34
	v_mov_b32_e32 v247, v35
	v_lshl_add_u64 v[250:251], v[36:37], 0, v[252:253]
	s_nop 1
	v_permlane16_swap_b32_e32 v244, v246
	v_permlane16_swap_b32_e32 v245, v247
	global_store_dwordx4 v[250:251], v[244:247], off nt
	v_lshlrev_b32_e32 v34, 16, v30
	v_and_b32_e32 v30, 0xffff0000, v30
	v_mul_f32_e32 v34, v126, v34
	v_mul_f32_e32 v30, v127, v30
	v_lshlrev_b32_e32 v35, 16, v31
	v_and_b32_e32 v31, 0xffff0000, v31
	v_lshlrev_b32_e32 v36, 16, v32
	v_and_b32_e32 v32, 0xffff0000, v32
	v_mul_f32_e32 v31, v129, v31
	v_mul_f32_e32 v36, v122, v36
	v_mul_f32_e32 v32, v123, v32
	v_mul_f32_e32 v34, 0x3c800000, v34
	v_mul_f32_e32 v30, 0x3c800000, v30
	v_mul_f32_e32 v31, 0x3c800000, v31
	v_mul_f32_e32 v36, 0x3c800000, v36
	v_mul_f32_e32 v32, 0x3c800000, v32
	v_med3_f32 v34, v34, s73, v227
	v_med3_f32 v38, v30, s73, v227
	v_mov_b32_e32 v30, v199
	v_med3_f32 v39, v31, s73, v227
	v_cvt_pk_fp8_f32 v30, v34, v38
	v_med3_f32 v34, v36, s73, v227
	v_med3_f32 v32, v32, s73, v227
	v_mov_b32_e32 v31, v199
	v_lshlrev_b32_e32 v37, 16, v33
	v_and_b32_e32 v33, 0xffff0000, v33
	v_cvt_pk_fp8_f32 v31, v34, v32
	v_mul_f32_e32 v35, v128, v35
	v_mul_f32_e32 v37, v124, v37
	v_mul_f32_e32 v33, v125, v33
	v_mul_f32_e32 v35, 0x3c800000, v35
	v_mul_f32_e32 v37, 0x3c800000, v37
	v_mul_f32_e32 v33, 0x3c800000, v33
	v_med3_f32 v35, v35, s73, v227
	v_med3_f32 v32, v37, s73, v227
	v_med3_f32 v33, v33, s73, v227
	v_cvt_pk_fp8_f32 v30, v35, v39 op_sel:[0,0,1]
	v_cvt_pk_fp8_f32 v31, v32, v33 op_sel:[0,0,1]
	v_lshlrev_b64 v[32:33], 11, v[52:53]
	v_lshl_add_u64 v[34:35], s[26:27], 0, v[32:33]
	v_lshl_add_u64 v[34:35], v[34:35], 0, v[210:211]
	v_mov_b32_e32 v240, v30
	v_mov_b32_e32 v241, v31
	v_lshlrev_b32_e32 v30, 16, v26
	v_and_b32_e32 v26, 0xffff0000, v26
	v_mul_f32_e32 v30, v118, v30
	v_mul_f32_e32 v26, v119, v26
	v_lshlrev_b32_e32 v31, 16, v27
	v_and_b32_e32 v27, 0xffff0000, v27
	v_lshlrev_b32_e32 v34, 16, v28
	v_and_b32_e32 v28, 0xffff0000, v28
	v_mul_f32_e32 v27, v121, v27
	v_mul_f32_e32 v34, v114, v34
	v_mul_f32_e32 v28, v115, v28
	v_mul_f32_e32 v30, 0x3c800000, v30
	v_mul_f32_e32 v26, 0x3c800000, v26
	v_mul_f32_e32 v27, 0x3c800000, v27
	v_mul_f32_e32 v34, 0x3c800000, v34
	v_mul_f32_e32 v28, 0x3c800000, v28
	v_med3_f32 v30, v30, s73, v227
	v_med3_f32 v36, v26, s73, v227
	v_mov_b32_e32 v26, v199
	v_med3_f32 v37, v27, s73, v227
	v_cvt_pk_fp8_f32 v26, v30, v36
	v_med3_f32 v30, v34, s73, v227
	v_med3_f32 v28, v28, s73, v227
	v_mov_b32_e32 v27, v199
	v_lshlrev_b32_e32 v35, 16, v29
	v_and_b32_e32 v29, 0xffff0000, v29
	v_cvt_pk_fp8_f32 v27, v30, v28
	v_mul_f32_e32 v31, v120, v31
	v_mul_f32_e32 v35, v116, v35
	v_mul_f32_e32 v29, v117, v29
	v_mul_f32_e32 v31, 0x3c800000, v31
	v_mul_f32_e32 v35, 0x3c800000, v35
	v_mul_f32_e32 v29, 0x3c800000, v29
	v_med3_f32 v31, v31, s73, v227
	v_med3_f32 v28, v35, s73, v227
	v_med3_f32 v29, v29, s73, v227
	v_cvt_pk_fp8_f32 v26, v31, v37 op_sel:[0,0,1]
	v_cvt_pk_fp8_f32 v27, v28, v29 op_sel:[0,0,1]
	v_lshl_add_u64 v[28:29], s[8:9], 0, v[32:33]
	v_lshl_add_u64 v[28:29], v[28:29], 0, v[210:211]
	v_add_co_u32_e32 v28, vcc, s74, v28
	s_nop 1
	v_addc_co_u32_e32 v29, vcc, 0, v29, vcc
	v_mov_b32_e32 v242, v26
	v_mov_b32_e32 v243, v27
	v_lshl_add_u64 v[248:249], v[28:29], 0, v[252:253]
	s_nop 1
	v_permlane16_swap_b32_e32 v240, v242
	v_permlane16_swap_b32_e32 v241, v243
	global_store_dwordx4 v[248:249], v[240:243], off nt
	v_lshlrev_b32_e32 v26, 16, v22
	v_and_b32_e32 v22, 0xffff0000, v22
	v_mul_f32_e32 v26, v110, v26
	v_mul_f32_e32 v22, v111, v22
	v_lshlrev_b32_e32 v27, 16, v23
	v_and_b32_e32 v23, 0xffff0000, v23
	v_lshlrev_b32_e32 v28, 16, v24
	v_and_b32_e32 v24, 0xffff0000, v24
	v_mul_f32_e32 v23, v113, v23
	v_mul_f32_e32 v28, v106, v28
	v_mul_f32_e32 v24, v107, v24
	v_mul_f32_e32 v26, 0x3c800000, v26
	v_mul_f32_e32 v22, 0x3c800000, v22
	v_mul_f32_e32 v23, 0x3c800000, v23
	v_mul_f32_e32 v28, 0x3c800000, v28
	v_mul_f32_e32 v24, 0x3c800000, v24
	v_med3_f32 v26, v26, s73, v227
	v_med3_f32 v30, v22, s73, v227
	v_mov_b32_e32 v22, v199
	v_med3_f32 v31, v23, s73, v227
	v_cvt_pk_fp8_f32 v22, v26, v30
	v_med3_f32 v26, v28, s73, v227
	v_med3_f32 v24, v24, s73, v227
	v_mov_b32_e32 v23, v199
	v_lshlrev_b32_e32 v29, 16, v25
	v_and_b32_e32 v25, 0xffff0000, v25
	v_cvt_pk_fp8_f32 v23, v26, v24
	v_mul_f32_e32 v27, v112, v27
	v_mul_f32_e32 v29, v108, v29
	v_mul_f32_e32 v25, v109, v25
	v_mul_f32_e32 v27, 0x3c800000, v27
	v_mul_f32_e32 v29, 0x3c800000, v29
	v_mul_f32_e32 v25, 0x3c800000, v25
	v_med3_f32 v27, v27, s73, v227
	v_med3_f32 v24, v29, s73, v227
	v_med3_f32 v25, v25, s73, v227
	v_cvt_pk_fp8_f32 v22, v27, v31 op_sel:[0,0,1]
	v_cvt_pk_fp8_f32 v23, v24, v25 op_sel:[0,0,1]
	v_lshlrev_b64 v[24:25], 11, v[50:51]
	v_lshl_add_u64 v[26:27], s[26:27], 0, v[24:25]
	v_lshl_add_u64 v[26:27], v[26:27], 0, v[210:211]
	v_mov_b32_e32 v244, v22
	v_mov_b32_e32 v245, v23
	v_lshlrev_b32_e32 v22, 16, v18
	v_and_b32_e32 v18, 0xffff0000, v18
	v_mul_f32_e32 v22, v102, v22
	v_mul_f32_e32 v18, v103, v18
	v_lshlrev_b32_e32 v23, 16, v19
	v_and_b32_e32 v19, 0xffff0000, v19
	v_lshlrev_b32_e32 v26, 16, v20
	v_and_b32_e32 v20, 0xffff0000, v20
	v_mul_f32_e32 v19, v105, v19
	v_mul_f32_e32 v26, v98, v26
	v_mul_f32_e32 v20, v99, v20
	v_mul_f32_e32 v22, 0x3c800000, v22
	v_mul_f32_e32 v18, 0x3c800000, v18
	v_mul_f32_e32 v19, 0x3c800000, v19
	v_mul_f32_e32 v26, 0x3c800000, v26
	v_mul_f32_e32 v20, 0x3c800000, v20
	v_med3_f32 v22, v22, s73, v227
	v_med3_f32 v28, v18, s73, v227
	v_mov_b32_e32 v18, v199
	v_med3_f32 v29, v19, s73, v227
	v_cvt_pk_fp8_f32 v18, v22, v28
	v_med3_f32 v22, v26, s73, v227
	v_med3_f32 v20, v20, s73, v227
	v_mov_b32_e32 v19, v199
	v_lshlrev_b32_e32 v27, 16, v21
	v_and_b32_e32 v21, 0xffff0000, v21
	v_cvt_pk_fp8_f32 v19, v22, v20
	v_mul_f32_e32 v23, v104, v23
	v_mul_f32_e32 v27, v100, v27
	v_mul_f32_e32 v21, v101, v21
	v_mul_f32_e32 v23, 0x3c800000, v23
	v_mul_f32_e32 v27, 0x3c800000, v27
	v_mul_f32_e32 v21, 0x3c800000, v21
	v_med3_f32 v23, v23, s73, v227
	v_med3_f32 v20, v27, s73, v227
	v_med3_f32 v21, v21, s73, v227
	v_cvt_pk_fp8_f32 v18, v23, v29 op_sel:[0,0,1]
	v_cvt_pk_fp8_f32 v19, v20, v21 op_sel:[0,0,1]
	v_lshl_add_u64 v[20:21], s[8:9], 0, v[24:25]
	v_lshl_add_u64 v[20:21], v[20:21], 0, v[210:211]
	v_add_co_u32_e32 v20, vcc, s74, v20
	s_nop 1
	v_addc_co_u32_e32 v21, vcc, 0, v21, vcc
	v_mov_b32_e32 v246, v18
	v_mov_b32_e32 v247, v19
	v_lshl_add_u64 v[250:251], v[20:21], 0, v[252:253]
	s_nop 1
	v_permlane16_swap_b32_e32 v244, v246
	v_permlane16_swap_b32_e32 v245, v247
	global_store_dwordx4 v[250:251], v[244:247], off nt
	v_lshlrev_b32_e32 v18, 16, v14
	v_and_b32_e32 v14, 0xffff0000, v14
	v_mul_f32_e32 v18, v94, v18
	v_mul_f32_e32 v14, v95, v14
	v_lshlrev_b32_e32 v19, 16, v15
	v_and_b32_e32 v15, 0xffff0000, v15
	v_lshlrev_b32_e32 v20, 16, v16
	v_and_b32_e32 v16, 0xffff0000, v16
	v_mul_f32_e32 v15, v97, v15
	v_mul_f32_e32 v20, v90, v20
	v_mul_f32_e32 v16, v91, v16
	v_mul_f32_e32 v18, 0x3c800000, v18
	v_mul_f32_e32 v14, 0x3c800000, v14
	v_mul_f32_e32 v15, 0x3c800000, v15
	v_mul_f32_e32 v20, 0x3c800000, v20
	v_mul_f32_e32 v16, 0x3c800000, v16
	v_med3_f32 v18, v18, s73, v227
	v_med3_f32 v22, v14, s73, v227
	v_mov_b32_e32 v14, v199
	v_med3_f32 v23, v15, s73, v227
	v_cvt_pk_fp8_f32 v14, v18, v22
	v_med3_f32 v18, v20, s73, v227
	v_med3_f32 v16, v16, s73, v227
	v_mov_b32_e32 v15, v199
	v_lshlrev_b32_e32 v21, 16, v17
	v_and_b32_e32 v17, 0xffff0000, v17
	v_cvt_pk_fp8_f32 v15, v18, v16
	v_mul_f32_e32 v19, v96, v19
	v_mul_f32_e32 v21, v92, v21
	v_mul_f32_e32 v17, v93, v17
	v_mul_f32_e32 v19, 0x3c800000, v19
	v_mul_f32_e32 v21, 0x3c800000, v21
	v_mul_f32_e32 v17, 0x3c800000, v17
	v_med3_f32 v19, v19, s73, v227
	v_med3_f32 v16, v21, s73, v227
	v_med3_f32 v17, v17, s73, v227
	v_cvt_pk_fp8_f32 v14, v19, v23 op_sel:[0,0,1]
	v_cvt_pk_fp8_f32 v15, v16, v17 op_sel:[0,0,1]
	v_lshlrev_b64 v[16:17], 11, v[48:49]
	v_lshl_add_u64 v[18:19], s[26:27], 0, v[16:17]
	v_lshl_add_u64 v[18:19], v[18:19], 0, v[210:211]
	v_mov_b32_e32 v240, v14
	v_mov_b32_e32 v241, v15
	v_lshlrev_b32_e32 v14, 16, v10
	v_and_b32_e32 v10, 0xffff0000, v10
	v_mul_f32_e32 v14, v86, v14
	v_mul_f32_e32 v10, v87, v10
	v_lshlrev_b32_e32 v15, 16, v11
	v_and_b32_e32 v11, 0xffff0000, v11
	v_lshlrev_b32_e32 v18, 16, v12
	v_and_b32_e32 v12, 0xffff0000, v12
	v_mul_f32_e32 v11, v89, v11
	v_mul_f32_e32 v18, v82, v18
	v_mul_f32_e32 v12, v83, v12
	v_mul_f32_e32 v14, 0x3c800000, v14
	v_mul_f32_e32 v10, 0x3c800000, v10
	v_mul_f32_e32 v11, 0x3c800000, v11
	v_mul_f32_e32 v18, 0x3c800000, v18
	v_mul_f32_e32 v12, 0x3c800000, v12
	v_med3_f32 v14, v14, s73, v227
	v_med3_f32 v20, v10, s73, v227
	v_mov_b32_e32 v10, v199
	v_med3_f32 v21, v11, s73, v227
	v_cvt_pk_fp8_f32 v10, v14, v20
	v_med3_f32 v14, v18, s73, v227
	v_med3_f32 v12, v12, s73, v227
	v_mov_b32_e32 v11, v199
	v_lshlrev_b32_e32 v19, 16, v13
	v_and_b32_e32 v13, 0xffff0000, v13
	v_cvt_pk_fp8_f32 v11, v14, v12
	v_mul_f32_e32 v15, v88, v15
	v_mul_f32_e32 v19, v84, v19
	v_mul_f32_e32 v13, v85, v13
	v_mul_f32_e32 v15, 0x3c800000, v15
	v_mul_f32_e32 v19, 0x3c800000, v19
	v_mul_f32_e32 v13, 0x3c800000, v13
	v_med3_f32 v15, v15, s73, v227
	v_med3_f32 v12, v19, s73, v227
	v_med3_f32 v13, v13, s73, v227
	v_cvt_pk_fp8_f32 v10, v15, v21 op_sel:[0,0,1]
	v_cvt_pk_fp8_f32 v11, v12, v13 op_sel:[0,0,1]
	v_lshl_add_u64 v[12:13], s[8:9], 0, v[16:17]
	v_lshl_add_u64 v[12:13], v[12:13], 0, v[210:211]
	v_add_co_u32_e32 v12, vcc, s74, v12
	s_nop 1
	v_addc_co_u32_e32 v13, vcc, 0, v13, vcc
	v_mov_b32_e32 v242, v10
	v_mov_b32_e32 v243, v11
	v_lshl_add_u64 v[248:249], v[12:13], 0, v[252:253]
	s_nop 1
	v_permlane16_swap_b32_e32 v240, v242
	v_permlane16_swap_b32_e32 v241, v243
	global_store_dwordx4 v[248:249], v[240:243], off nt
	v_lshlrev_b32_e32 v10, 16, v6
	v_and_b32_e32 v6, 0xffff0000, v6
	v_mul_f32_e32 v10, v78, v10
	v_mul_f32_e32 v6, v79, v6
	v_lshlrev_b32_e32 v11, 16, v7
	v_and_b32_e32 v7, 0xffff0000, v7
	v_lshlrev_b32_e32 v12, 16, v8
	v_and_b32_e32 v8, 0xffff0000, v8
	v_mul_f32_e32 v7, v81, v7
	v_mul_f32_e32 v12, v74, v12
	v_mul_f32_e32 v8, v75, v8
	v_mul_f32_e32 v10, 0x3c800000, v10
	v_mul_f32_e32 v6, 0x3c800000, v6
	v_mul_f32_e32 v7, 0x3c800000, v7
	v_mul_f32_e32 v12, 0x3c800000, v12
	v_mul_f32_e32 v8, 0x3c800000, v8
	v_med3_f32 v10, v10, s73, v227
	v_med3_f32 v14, v6, s73, v227
	v_mov_b32_e32 v6, v199
	v_med3_f32 v15, v7, s73, v227
	v_cvt_pk_fp8_f32 v6, v10, v14
	v_med3_f32 v10, v12, s73, v227
	v_med3_f32 v8, v8, s73, v227
	v_mov_b32_e32 v7, v199
	v_lshlrev_b32_e32 v13, 16, v9
	v_and_b32_e32 v9, 0xffff0000, v9
	v_cvt_pk_fp8_f32 v7, v10, v8
	v_mul_f32_e32 v11, v80, v11
	v_mul_f32_e32 v13, v76, v13
	v_mul_f32_e32 v9, v77, v9
	v_mul_f32_e32 v11, 0x3c800000, v11
	v_mul_f32_e32 v13, 0x3c800000, v13
	v_mul_f32_e32 v9, 0x3c800000, v9
	v_med3_f32 v11, v11, s73, v227
	v_med3_f32 v8, v13, s73, v227
	v_med3_f32 v9, v9, s73, v227
	v_cvt_pk_fp8_f32 v6, v11, v15 op_sel:[0,0,1]
	v_cvt_pk_fp8_f32 v7, v8, v9 op_sel:[0,0,1]
	v_lshlrev_b64 v[8:9], 11, v[46:47]
	v_lshl_add_u64 v[10:11], s[26:27], 0, v[8:9]
	v_lshl_add_u64 v[10:11], v[10:11], 0, v[210:211]
	v_mov_b32_e32 v244, v6
	v_mov_b32_e32 v245, v7
	v_lshlrev_b32_e32 v6, 16, v2
	v_and_b32_e32 v2, 0xffff0000, v2
	v_mul_f32_e32 v6, v70, v6
	v_mul_f32_e32 v2, v71, v2
	v_lshlrev_b32_e32 v7, 16, v3
	v_and_b32_e32 v3, 0xffff0000, v3
	v_lshlrev_b32_e32 v10, 16, v4
	v_and_b32_e32 v4, 0xffff0000, v4
	v_mul_f32_e32 v3, v73, v3
	v_mul_f32_e32 v10, v66, v10
	v_mul_f32_e32 v4, v67, v4
	v_mul_f32_e32 v6, 0x3c800000, v6
	v_mul_f32_e32 v2, 0x3c800000, v2
	v_mul_f32_e32 v3, 0x3c800000, v3
	v_mul_f32_e32 v10, 0x3c800000, v10
	v_mul_f32_e32 v4, 0x3c800000, v4
	v_med3_f32 v6, v6, s73, v227
	v_med3_f32 v12, v2, s73, v227
	v_mov_b32_e32 v2, v199
	v_med3_f32 v13, v3, s73, v227
	v_cvt_pk_fp8_f32 v2, v6, v12
	v_med3_f32 v6, v10, s73, v227
	v_med3_f32 v4, v4, s73, v227
	v_mov_b32_e32 v3, v199
	v_lshlrev_b32_e32 v11, 16, v5
	v_and_b32_e32 v5, 0xffff0000, v5
	v_cvt_pk_fp8_f32 v3, v6, v4
	v_mul_f32_e32 v11, v68, v11
	v_mul_f32_e32 v5, v69, v5
	v_mul_f32_e32 v7, v72, v7
	v_mul_f32_e32 v11, 0x3c800000, v11
	v_mul_f32_e32 v5, 0x3c800000, v5
	v_mul_f32_e32 v7, 0x3c800000, v7
	v_med3_f32 v4, v11, s73, v227
	v_med3_f32 v5, v5, s73, v227
	v_med3_f32 v7, v7, s73, v227
	v_cvt_pk_fp8_f32 v3, v4, v5 op_sel:[0,0,1]
	v_lshl_add_u64 v[4:5], s[8:9], 0, v[8:9]
	v_cvt_pk_fp8_f32 v2, v7, v13 op_sel:[0,0,1]
	v_lshl_add_u64 v[4:5], v[4:5], 0, v[210:211]
	v_add_co_u32_e32 v4, vcc, 0x24c00000, v4
	s_nop 1
	v_addc_co_u32_e32 v5, vcc, 0, v5, vcc
	s_and_b64 vcc, exec, s[0:1]
	s_mov_b64 s[0:1], -1
	v_mov_b32_e32 v246, v2
	v_mov_b32_e32 v247, v3
	v_lshl_add_u64 v[250:251], v[4:5], 0, v[252:253]
	s_nop 1
	v_permlane16_swap_b32_e32 v244, v246
	v_permlane16_swap_b32_e32 v245, v247
	global_store_dwordx4 v[250:251], v[244:247], off nt
	s_cbranch_vccnz .LBB0_1098
	s_andn2_b64 vcc, exec, s[16:17]
	s_cbranch_vccnz .LBB0_1097
	s_barrier
	s_branch .LBB0_1097

.LBB0_1196:
	v_lshl_add_u32 v10, s59, 8, v219
	v_lshl_or_b32 v2, s60, 8, v221
	v_ashrrev_i32_e32 v11, 31, v10
	v_ashrrev_i32_e32 v3, 31, v2
	v_lshlrev_b64 v[4:5], 12, v[10:11]
	v_lshl_add_u64 v[6:7], s[22:23], 0, v[4:5]
	v_lshlrev_b64 v[2:3], 1, v[2:3]
	v_mul_f32_e32 v8, 0x3c800000, v190
	v_mul_f32_e32 v9, 0x3c800000, v191
	v_mul_f32_e32 v11, 0x3c800000, v192
	v_mul_f32_e32 v14, 0x3c800000, v193
	v_lshl_add_u64 v[12:13], v[6:7], 0, v[2:3]
	v_cvt_pk_bf16_f32 v6, v8, v9
	v_cvt_pk_bf16_f32 v7, v11, v14
	v_mul_f32_e32 v15, 0x3c800000, v186
	v_mul_f32_e32 v16, 0x3c800000, v187
	v_mul_f32_e32 v17, 0x3c800000, v188
	v_mul_f32_e32 v18, 0x3c800000, v189
	v_cvt_pk_bf16_f32 v8, v15, v16
	v_cvt_pk_bf16_f32 v9, v17, v18
	global_store_dwordx4 v[12:13], v[6:9], off nt
	v_mul_f32_e32 v11, 0x3c800000, v184
	v_mul_f32_e32 v14, 0x3c800000, v185
	v_lshl_add_u64 v[6:7], s[8:9], 0, v[4:5]
	v_lshl_add_u64 v[12:13], v[6:7], 0, v[2:3]
	v_add_co_u32_e32 v12, vcc, s56, v12
	v_mul_f32_e32 v8, 0x3c800000, v182
	v_mul_f32_e32 v9, 0x3c800000, v183
	v_cvt_pk_bf16_f32 v6, v8, v9
	v_addc_co_u32_e32 v13, vcc, 0, v13, vcc
	v_mul_f32_e32 v15, 0x3c800000, v174
	v_mul_f32_e32 v16, 0x3c800000, v175
	v_mul_f32_e32 v17, 0x3c800000, v176
	v_mul_f32_e32 v18, 0x3c800000, v177
	v_cvt_pk_bf16_f32 v7, v11, v14
	v_cvt_pk_bf16_f32 v8, v15, v16
	v_cvt_pk_bf16_f32 v9, v17, v18
	global_store_dwordx4 v[12:13], v[6:9], off offset:256
	v_mul_f32_e32 v11, 0x3c800000, v180
	v_mul_f32_e32 v16, 0x3c800000, v181
	v_or_b32_e32 v6, 16, v10
	v_ashrrev_i32_e32 v7, 31, v6
	v_lshlrev_b64 v[12:13], 12, v[6:7]
	v_lshl_add_u64 v[6:7], s[22:23], 0, v[12:13]
	v_mul_f32_e32 v8, 0x3c800000, v178
	v_mul_f32_e32 v9, 0x3c800000, v179
	v_lshl_add_u64 v[14:15], v[6:7], 0, v[2:3]
	v_cvt_pk_bf16_f32 v6, v8, v9
	v_cvt_pk_bf16_f32 v7, v11, v16
	v_mul_f32_e32 v17, 0x3c800000, v170
	v_mul_f32_e32 v18, 0x3c800000, v171
	v_mul_f32_e32 v19, 0x3c800000, v172
	v_mul_f32_e32 v20, 0x3c800000, v173
	v_cvt_pk_bf16_f32 v8, v17, v18
	v_cvt_pk_bf16_f32 v9, v19, v20
	global_store_dwordx4 v[14:15], v[6:9], off nt
	v_mul_f32_e32 v11, 0x3c800000, v168
	v_mul_f32_e32 v14, 0x3c800000, v169
	v_lshl_add_u64 v[6:7], s[8:9], 0, v[12:13]
	v_lshl_add_u64 v[12:13], v[6:7], 0, v[2:3]
	v_add_co_u32_e32 v12, vcc, s56, v12
	v_mul_f32_e32 v8, 0x3c800000, v166
	v_mul_f32_e32 v9, 0x3c800000, v167
	v_cvt_pk_bf16_f32 v6, v8, v9
	v_addc_co_u32_e32 v13, vcc, 0, v13, vcc
	v_mul_f32_e32 v15, 0x3c800000, v158
	v_mul_f32_e32 v16, 0x3c800000, v159
	v_mul_f32_e32 v17, 0x3c800000, v160
	v_mul_f32_e32 v18, 0x3c800000, v161
	v_cvt_pk_bf16_f32 v7, v11, v14
	v_cvt_pk_bf16_f32 v8, v15, v16
	v_cvt_pk_bf16_f32 v9, v17, v18
	global_store_dwordx4 v[12:13], v[6:9], off offset:256
	v_mul_f32_e32 v11, 0x3c800000, v164
	v_mul_f32_e32 v16, 0x3c800000, v165
	v_or_b32_e32 v6, 32, v10
	v_ashrrev_i32_e32 v7, 31, v6
	v_lshlrev_b64 v[12:13], 12, v[6:7]
	v_lshl_add_u64 v[6:7], s[22:23], 0, v[12:13]
	v_mul_f32_e32 v8, 0x3c800000, v162
	v_mul_f32_e32 v9, 0x3c800000, v163
	v_lshl_add_u64 v[14:15], v[6:7], 0, v[2:3]
	v_cvt_pk_bf16_f32 v6, v8, v9
	v_cvt_pk_bf16_f32 v7, v11, v16
	v_mul_f32_e32 v17, 0x3c800000, v154
	v_mul_f32_e32 v18, 0x3c800000, v155
	v_mul_f32_e32 v19, 0x3c800000, v156
	v_mul_f32_e32 v20, 0x3c800000, v157
	v_cvt_pk_bf16_f32 v8, v17, v18
	v_cvt_pk_bf16_f32 v9, v19, v20
	global_store_dwordx4 v[14:15], v[6:9], off nt
	v_mul_f32_e32 v11, 0x3c800000, v152
	v_mul_f32_e32 v14, 0x3c800000, v153
	v_lshl_add_u64 v[6:7], s[8:9], 0, v[12:13]
	v_lshl_add_u64 v[12:13], v[6:7], 0, v[2:3]
	v_add_co_u32_e32 v12, vcc, s56, v12
	v_mul_f32_e32 v8, 0x3c800000, v150
	v_mul_f32_e32 v9, 0x3c800000, v151
	v_cvt_pk_bf16_f32 v6, v8, v9
	v_addc_co_u32_e32 v13, vcc, 0, v13, vcc
	v_mul_f32_e32 v15, 0x3c800000, v142
	v_mul_f32_e32 v16, 0x3c800000, v143
	v_mul_f32_e32 v17, 0x3c800000, v144
	v_mul_f32_e32 v18, 0x3c800000, v145
	v_cvt_pk_bf16_f32 v7, v11, v14
	v_cvt_pk_bf16_f32 v8, v15, v16
	v_cvt_pk_bf16_f32 v9, v17, v18
	global_store_dwordx4 v[12:13], v[6:9], off offset:256
	v_mul_f32_e32 v14, 0x3c800000, v148
	v_mul_f32_e32 v15, 0x3c800000, v149
	v_or_b32_e32 v6, 48, v10
	v_ashrrev_i32_e32 v7, 31, v6
	v_lshlrev_b64 v[10:11], 12, v[6:7]
	v_lshl_add_u64 v[6:7], s[22:23], 0, v[10:11]
	v_mul_f32_e32 v8, 0x3c800000, v146
	v_mul_f32_e32 v9, 0x3c800000, v147
	v_lshl_add_u64 v[12:13], v[6:7], 0, v[2:3]
	v_cvt_pk_bf16_f32 v6, v8, v9
	v_cvt_pk_bf16_f32 v7, v14, v15
	v_mul_f32_e32 v16, 0x3c800000, v138
	v_mul_f32_e32 v17, 0x3c800000, v139
	v_mul_f32_e32 v18, 0x3c800000, v140
	v_mul_f32_e32 v19, 0x3c800000, v141
	v_cvt_pk_bf16_f32 v8, v16, v17
	v_cvt_pk_bf16_f32 v9, v18, v19
	global_store_dwordx4 v[12:13], v[6:9], off nt
	v_mul_f32_e32 v12, 0x3c800000, v136
	v_mul_f32_e32 v13, 0x3c800000, v137
	v_lshl_add_u64 v[6:7], s[8:9], 0, v[10:11]
	v_lshl_add_u64 v[10:11], v[6:7], 0, v[2:3]
	v_add_co_u32_e32 v10, vcc, s56, v10
	v_mul_f32_e32 v8, 0x3c800000, v134
	v_mul_f32_e32 v9, 0x3c800000, v135
	v_addc_co_u32_e32 v11, vcc, 0, v11, vcc
	v_mul_f32_e32 v14, 0x3c800000, v130
	v_mul_f32_e32 v15, 0x3c800000, v131
	v_mul_f32_e32 v16, 0x3c800000, v132
	v_mul_f32_e32 v17, 0x3c800000, v133
	v_cvt_pk_bf16_f32 v6, v8, v9
	v_cvt_pk_bf16_f32 v7, v12, v13
	v_cvt_pk_bf16_f32 v8, v14, v15
	v_cvt_pk_bf16_f32 v9, v16, v17
	global_store_dwordx4 v[10:11], v[6:9], off offset:256
	v_lshl_add_u64 v[10:11], v[4:5], 0, s[24:25]
	v_mul_f32_e32 v14, 0x3c800000, v128
	v_lshl_add_u64 v[6:7], s[22:23], 0, v[10:11]
	v_mul_f32_e32 v8, 0x3c800000, v126
	v_mul_f32_e32 v9, 0x3c800000, v127
	v_mul_f32_e32 v15, 0x3c800000, v129
	v_lshl_add_u64 v[12:13], v[6:7], 0, v[2:3]
	v_cvt_pk_bf16_f32 v6, v8, v9
	v_cvt_pk_bf16_f32 v7, v14, v15
	v_mul_f32_e32 v16, 0x3c800000, v122
	v_mul_f32_e32 v17, 0x3c800000, v123
	v_mul_f32_e32 v18, 0x3c800000, v124
	v_mul_f32_e32 v19, 0x3c800000, v125
	v_cvt_pk_bf16_f32 v8, v16, v17
	v_cvt_pk_bf16_f32 v9, v18, v19
	global_store_dwordx4 v[12:13], v[6:9], off nt
	v_mul_f32_e32 v12, 0x3c800000, v116
	v_mul_f32_e32 v13, 0x3c800000, v117
	v_lshl_add_u64 v[6:7], s[8:9], 0, v[10:11]
	v_lshl_add_u64 v[10:11], v[6:7], 0, v[2:3]
	v_add_co_u32_e32 v10, vcc, s56, v10
	v_mul_f32_e32 v8, 0x3c800000, v114
	v_mul_f32_e32 v9, 0x3c800000, v115
	v_addc_co_u32_e32 v11, vcc, 0, v11, vcc
	v_mul_f32_e32 v14, 0x3c800000, v106
	v_mul_f32_e32 v15, 0x3c800000, v107
	v_mul_f32_e32 v16, 0x3c800000, v108
	v_mul_f32_e32 v17, 0x3c800000, v109
	v_cvt_pk_bf16_f32 v6, v8, v9
	v_cvt_pk_bf16_f32 v7, v12, v13
	v_cvt_pk_bf16_f32 v8, v14, v15
	v_cvt_pk_bf16_f32 v9, v16, v17
	global_store_dwordx4 v[10:11], v[6:9], off offset:256
	v_lshl_add_u64 v[10:11], v[4:5], 0, s[26:27]
	v_mul_f32_e32 v14, 0x3c800000, v120
	v_lshl_add_u64 v[6:7], s[22:23], 0, v[10:11]
	v_mul_f32_e32 v8, 0x3c800000, v118
	v_mul_f32_e32 v9, 0x3c800000, v119
	v_mul_f32_e32 v15, 0x3c800000, v121
	v_lshl_add_u64 v[12:13], v[6:7], 0, v[2:3]
	v_cvt_pk_bf16_f32 v6, v8, v9
	v_cvt_pk_bf16_f32 v7, v14, v15
	v_mul_f32_e32 v16, 0x3c800000, v110
	v_mul_f32_e32 v17, 0x3c800000, v111
	v_mul_f32_e32 v18, 0x3c800000, v112
	v_mul_f32_e32 v19, 0x3c800000, v113
	v_cvt_pk_bf16_f32 v8, v16, v17
	v_cvt_pk_bf16_f32 v9, v18, v19
	global_store_dwordx4 v[12:13], v[6:9], off nt
	v_mul_f32_e32 v12, 0x3c800000, v100
	v_mul_f32_e32 v13, 0x3c800000, v101
	v_lshl_add_u64 v[6:7], s[8:9], 0, v[10:11]
	v_lshl_add_u64 v[10:11], v[6:7], 0, v[2:3]
	v_add_co_u32_e32 v10, vcc, s56, v10
	v_mul_f32_e32 v8, 0x3c800000, v98
	v_mul_f32_e32 v9, 0x3c800000, v99
	v_addc_co_u32_e32 v11, vcc, 0, v11, vcc
	v_mul_f32_e32 v14, 0x3c800000, v90
	v_mul_f32_e32 v15, 0x3c800000, v91
	v_mul_f32_e32 v16, 0x3c800000, v92
	v_mul_f32_e32 v17, 0x3c800000, v93
	v_cvt_pk_bf16_f32 v6, v8, v9
	v_cvt_pk_bf16_f32 v7, v12, v13
	v_cvt_pk_bf16_f32 v8, v14, v15
	v_cvt_pk_bf16_f32 v9, v16, v17
	global_store_dwordx4 v[10:11], v[6:9], off offset:256
	v_lshl_add_u64 v[10:11], v[4:5], 0, s[28:29]
	v_mul_f32_e32 v14, 0x3c800000, v104
	v_lshl_add_u64 v[6:7], s[22:23], 0, v[10:11]
	v_mul_f32_e32 v8, 0x3c800000, v102
	v_mul_f32_e32 v9, 0x3c800000, v103
	v_mul_f32_e32 v15, 0x3c800000, v105
	v_lshl_add_u64 v[12:13], v[6:7], 0, v[2:3]
	v_cvt_pk_bf16_f32 v6, v8, v9
	v_cvt_pk_bf16_f32 v7, v14, v15
	v_mul_f32_e32 v16, 0x3c800000, v94
	v_mul_f32_e32 v17, 0x3c800000, v95
	v_mul_f32_e32 v18, 0x3c800000, v96
	v_mul_f32_e32 v19, 0x3c800000, v97
	v_cvt_pk_bf16_f32 v8, v16, v17
	v_cvt_pk_bf16_f32 v9, v18, v19
	global_store_dwordx4 v[12:13], v[6:9], off nt
	v_mul_f32_e32 v14, 0x3c800000, v74
	v_mul_f32_e32 v15, 0x3c800000, v75
	v_lshl_add_u64 v[6:7], s[8:9], 0, v[10:11]
	v_lshl_add_u64 v[10:11], v[6:7], 0, v[2:3]
	v_mul_f32_e32 v8, 0x3c800000, v82
	v_mul_f32_e32 v9, 0x3c800000, v83
	v_add_co_u32_e32 v10, vcc, s56, v10
	v_mul_f32_e32 v16, 0x3c800000, v76
	v_mul_f32_e32 v17, 0x3c800000, v77
	v_cvt_pk_bf16_f32 v6, v8, v9
	v_cvt_pk_bf16_f32 v8, v14, v15
	v_cvt_pk_bf16_f32 v9, v16, v17
	v_addc_co_u32_e32 v11, vcc, 0, v11, vcc
	v_mul_f32_e32 v12, 0x3c800000, v84
	v_mul_f32_e32 v13, 0x3c800000, v85
	v_cvt_pk_bf16_f32 v7, v12, v13
	global_store_dwordx4 v[10:11], v[6:9], off offset:256
	v_mul_f32_e32 v12, 0x3c800000, v88
	v_mul_f32_e32 v13, 0x3c800000, v89
	v_lshl_add_u64 v[8:9], v[4:5], 0, s[30:31]
	v_lshl_add_u64 v[4:5], s[22:23], 0, v[8:9]
	v_mul_f32_e32 v6, 0x3c800000, v86
	v_mul_f32_e32 v7, 0x3c800000, v87
	v_lshl_add_u64 v[10:11], v[4:5], 0, v[2:3]
	v_cvt_pk_bf16_f32 v4, v6, v7
	v_cvt_pk_bf16_f32 v5, v12, v13
	v_mul_f32_e32 v14, 0x3c800000, v78
	v_mul_f32_e32 v15, 0x3c800000, v79
	v_mul_f32_e32 v16, 0x3c800000, v80
	v_mul_f32_e32 v17, 0x3c800000, v81
	v_cvt_pk_bf16_f32 v6, v14, v15
	v_cvt_pk_bf16_f32 v7, v16, v17
	global_store_dwordx4 v[10:11], v[4:7], off nt
	v_mul_f32_e32 v10, 0x3c800000, v70
	v_mul_f32_e32 v11, 0x3c800000, v71
	v_lshl_add_u64 v[4:5], s[8:9], 0, v[8:9]
	v_lshl_add_u64 v[6:7], v[4:5], 0, v[2:3]
	v_add_co_u32_e32 v6, vcc, 0x28c00000, v6
	v_mul_f32_e32 v12, 0x3c800000, v72
	s_nop 0
	v_addc_co_u32_e32 v7, vcc, 0, v7, vcc
	s_and_b64 vcc, exec, s[0:1]
	s_mov_b64 s[0:1], -1
	v_mul_f32_e32 v13, 0x3c800000, v73
	v_mul_f32_e32 v14, 0x3c800000, v66
	v_mul_f32_e32 v15, 0x3c800000, v67
	v_mul_f32_e32 v16, 0x3c800000, v68
	v_mul_f32_e32 v17, 0x3c800000, v69
	v_cvt_pk_bf16_f32 v2, v10, v11
	v_cvt_pk_bf16_f32 v3, v12, v13
	v_cvt_pk_bf16_f32 v4, v14, v15
	v_cvt_pk_bf16_f32 v5, v16, v17
	global_store_dwordx4 v[6:7], v[2:5], off offset:256
	s_cbranch_vccnz .LBB0_1180
	s_andn2_b64 vcc, exec, s[16:17]
	s_cbranch_vccnz .LBB0_1179
	s_barrier
	s_branch .LBB0_1179

.LBB0_1487:
	v_mul_f32_e32 v4, 0x3e000000, v189
	v_med3_f32 v6, v4, s58, v237
	v_mul_f32_e32 v4, 0x3e000000, v190
	v_med3_f32 v5, v4, s58, v237
	v_mul_f32_e32 v4, 0x3e000000, v191
	v_med3_f32 v7, v4, s58, v237
	v_mul_f32_e32 v4, 0x3e000000, v192
	v_med3_f32 v8, v4, s58, v237
	v_mul_f32_e32 v4, 0x3e000000, v193
	v_med3_f32 v9, v4, s58, v237
	v_mul_f32_e32 v4, 0x3e000000, v186
	v_med3_f32 v10, v4, s58, v237
	v_mul_f32_e32 v4, 0x3e000000, v187
	v_med3_f32 v11, v4, s58, v237
	v_mov_b32_e32 v4, v199
	v_cvt_pk_fp8_f32 v4, v5, v7
	v_mov_b32_e32 v5, v199
	v_cvt_pk_fp8_f32 v5, v10, v11
	v_mul_f32_e32 v7, 0x3e000000, v188
	v_cvt_pk_fp8_f32 v4, v8, v9 op_sel:[0,0,1]
	v_mul_f32_e32 v8, 0x3e000000, v177
	v_med3_f32 v10, v8, s58, v237
	v_mul_f32_e32 v8, 0x3e000000, v182
	v_med3_f32 v9, v8, s58, v237
	v_mul_f32_e32 v8, 0x3e000000, v183
	v_med3_f32 v11, v8, s58, v237
	v_mul_f32_e32 v8, 0x3e000000, v184
	v_med3_f32 v12, v8, s58, v237
	v_mul_f32_e32 v8, 0x3e000000, v185
	v_med3_f32 v13, v8, s58, v237
	v_mul_f32_e32 v8, 0x3e000000, v174
	v_med3_f32 v14, v8, s58, v237
	v_mul_f32_e32 v8, 0x3e000000, v175
	v_med3_f32 v15, v8, s58, v237
	v_mov_b32_e32 v8, v199
	v_cvt_pk_fp8_f32 v8, v9, v11
	v_mov_b32_e32 v9, v199
	v_cvt_pk_fp8_f32 v9, v14, v15
	v_med3_f32 v7, v7, s58, v237
	v_mul_f32_e32 v11, 0x3e000000, v176
	v_cvt_pk_fp8_f32 v5, v7, v6 op_sel:[0,0,1]
	v_add_u32_e32 v6, v221, v225
	v_med3_f32 v11, v11, s58, v237
	v_ashrrev_i32_e32 v7, 31, v6
	v_cvt_pk_fp8_f32 v8, v12, v13 op_sel:[0,0,1]
	v_cvt_pk_fp8_f32 v9, v11, v10 op_sel:[0,0,1]
	v_lshlrev_b64 v[6:7], 11, v[6:7]
	v_lshl_add_u64 v[6:7], v[2:3], 0, v[6:7]
	v_mov_b32_e32 v40, v4
	v_mov_b32_e32 v41, v5
	v_mov_b32_e32 v42, v8
	v_mov_b32_e32 v43, v9
	v_lshl_add_u64 v[48:49], v[6:7], 0, v[52:53]
	s_nop 1
	v_permlane16_swap_b32_e32 v40, v42
	v_permlane16_swap_b32_e32 v41, v43
	global_store_dwordx4 v[48:49], v[40:43], off nt
	s_or_b64 exec, exec, s[4:5]
	v_cmp_lt_i32_e32 vcc, v227, v224
	s_and_saveexec_b64 s[4:5], vcc
	s_cbranch_execz .LBB0_1480
.LBB0_1488:
	v_mul_f32_e32 v4, 0x3e000000, v173
	v_med3_f32 v6, v4, s58, v237
	v_mul_f32_e32 v4, 0x3e000000, v178
	v_med3_f32 v5, v4, s58, v237
	v_mul_f32_e32 v4, 0x3e000000, v179
	v_med3_f32 v7, v4, s58, v237
	v_mul_f32_e32 v4, 0x3e000000, v180
	v_med3_f32 v8, v4, s58, v237
	v_mul_f32_e32 v4, 0x3e000000, v181
	v_med3_f32 v9, v4, s58, v237
	v_mul_f32_e32 v4, 0x3e000000, v170
	v_med3_f32 v10, v4, s58, v237
	v_mul_f32_e32 v4, 0x3e000000, v171
	v_med3_f32 v11, v4, s58, v237
	v_mov_b32_e32 v4, v199
	v_cvt_pk_fp8_f32 v4, v5, v7
	v_mov_b32_e32 v5, v199
	v_cvt_pk_fp8_f32 v5, v10, v11
	v_mul_f32_e32 v7, 0x3e000000, v172
	v_cvt_pk_fp8_f32 v4, v8, v9 op_sel:[0,0,1]
	v_mul_f32_e32 v8, 0x3e000000, v161
	v_med3_f32 v10, v8, s58, v237
	v_mul_f32_e32 v8, 0x3e000000, v166
	v_med3_f32 v9, v8, s58, v237
	v_mul_f32_e32 v8, 0x3e000000, v167
	v_med3_f32 v11, v8, s58, v237
	v_mul_f32_e32 v8, 0x3e000000, v168
	v_med3_f32 v12, v8, s58, v237
	v_mul_f32_e32 v8, 0x3e000000, v169
	v_med3_f32 v13, v8, s58, v237
	v_mul_f32_e32 v8, 0x3e000000, v158
	v_med3_f32 v14, v8, s58, v237
	v_mul_f32_e32 v8, 0x3e000000, v159
	v_med3_f32 v15, v8, s58, v237
	v_mov_b32_e32 v8, v199
	v_cvt_pk_fp8_f32 v8, v9, v11
	v_mov_b32_e32 v9, v199
	v_cvt_pk_fp8_f32 v9, v14, v15
	v_med3_f32 v7, v7, s58, v237
	v_mul_f32_e32 v11, 0x3e000000, v160
	v_cvt_pk_fp8_f32 v5, v7, v6 op_sel:[0,0,1]
	v_add_u32_e32 v6, v221, v227
	v_med3_f32 v11, v11, s58, v237
	v_ashrrev_i32_e32 v7, 31, v6
	v_cvt_pk_fp8_f32 v8, v12, v13 op_sel:[0,0,1]
	v_cvt_pk_fp8_f32 v9, v11, v10 op_sel:[0,0,1]
	v_lshlrev_b64 v[6:7], 11, v[6:7]
	v_lshl_add_u64 v[6:7], v[2:3], 0, v[6:7]
	v_mov_b32_e32 v44, v4
	v_mov_b32_e32 v45, v5
	v_mov_b32_e32 v46, v8
	v_mov_b32_e32 v47, v9
	v_lshl_add_u64 v[50:51], v[6:7], 0, v[52:53]
	s_nop 1
	v_permlane16_swap_b32_e32 v44, v46
	v_permlane16_swap_b32_e32 v45, v47
	global_store_dwordx4 v[50:51], v[44:47], off nt
	s_or_b64 exec, exec, s[4:5]
	v_cmp_lt_i32_e32 vcc, v228, v224
	s_and_saveexec_b64 s[4:5], vcc
	s_cbranch_execz .LBB0_1481
.LBB0_1489:
	v_mul_f32_e32 v4, 0x3e000000, v157
	v_med3_f32 v6, v4, s58, v237
	v_mul_f32_e32 v4, 0x3e000000, v162
	v_med3_f32 v5, v4, s58, v237
	v_mul_f32_e32 v4, 0x3e000000, v163
	v_med3_f32 v7, v4, s58, v237
	v_mul_f32_e32 v4, 0x3e000000, v164
	v_med3_f32 v8, v4, s58, v237
	v_mul_f32_e32 v4, 0x3e000000, v165
	v_med3_f32 v9, v4, s58, v237
	v_mul_f32_e32 v4, 0x3e000000, v154
	v_med3_f32 v10, v4, s58, v237
	v_mul_f32_e32 v4, 0x3e000000, v155
	v_med3_f32 v11, v4, s58, v237
	v_mov_b32_e32 v4, v199
	v_cvt_pk_fp8_f32 v4, v5, v7
	v_mov_b32_e32 v5, v199
	v_cvt_pk_fp8_f32 v5, v10, v11
	v_mul_f32_e32 v7, 0x3e000000, v156
	v_cvt_pk_fp8_f32 v4, v8, v9 op_sel:[0,0,1]
	v_mul_f32_e32 v8, 0x3e000000, v145
	v_med3_f32 v10, v8, s58, v237
	v_mul_f32_e32 v8, 0x3e000000, v150
	v_med3_f32 v9, v8, s58, v237
	v_mul_f32_e32 v8, 0x3e000000, v151
	v_med3_f32 v11, v8, s58, v237
	v_mul_f32_e32 v8, 0x3e000000, v152
	v_med3_f32 v12, v8, s58, v237
	v_mul_f32_e32 v8, 0x3e000000, v153
	v_med3_f32 v13, v8, s58, v237
	v_mul_f32_e32 v8, 0x3e000000, v142
	v_med3_f32 v14, v8, s58, v237
	v_mul_f32_e32 v8, 0x3e000000, v143
	v_med3_f32 v15, v8, s58, v237
	v_mov_b32_e32 v8, v199
	v_cvt_pk_fp8_f32 v8, v9, v11
	v_mov_b32_e32 v9, v199
	v_cvt_pk_fp8_f32 v9, v14, v15
	v_med3_f32 v7, v7, s58, v237
	v_mul_f32_e32 v11, 0x3e000000, v144
	v_cvt_pk_fp8_f32 v5, v7, v6 op_sel:[0,0,1]
	v_add_u32_e32 v6, v221, v228
	v_med3_f32 v11, v11, s58, v237
	v_ashrrev_i32_e32 v7, 31, v6
	v_cvt_pk_fp8_f32 v8, v12, v13 op_sel:[0,0,1]
	v_cvt_pk_fp8_f32 v9, v11, v10 op_sel:[0,0,1]
	v_lshlrev_b64 v[6:7], 11, v[6:7]
	v_lshl_add_u64 v[6:7], v[2:3], 0, v[6:7]
	v_mov_b32_e32 v40, v4
	v_mov_b32_e32 v41, v5
	v_mov_b32_e32 v42, v8
	v_mov_b32_e32 v43, v9
	v_lshl_add_u64 v[48:49], v[6:7], 0, v[52:53]
	s_nop 1
	v_permlane16_swap_b32_e32 v40, v42
	v_permlane16_swap_b32_e32 v41, v43
	global_store_dwordx4 v[48:49], v[40:43], off nt
	s_or_b64 exec, exec, s[4:5]
	v_cmp_lt_i32_e32 vcc, v229, v224
	s_and_saveexec_b64 s[4:5], vcc
	s_cbranch_execz .LBB0_1482
.LBB0_1490:
	v_mul_f32_e32 v4, 0x3e000000, v141
	v_med3_f32 v6, v4, s58, v237
	v_mul_f32_e32 v4, 0x3e000000, v146
	v_med3_f32 v5, v4, s58, v237
	v_mul_f32_e32 v4, 0x3e000000, v147
	v_med3_f32 v7, v4, s58, v237
	v_mul_f32_e32 v4, 0x3e000000, v148
	v_med3_f32 v8, v4, s58, v237
	v_mul_f32_e32 v4, 0x3e000000, v149
	v_med3_f32 v9, v4, s58, v237
	v_mul_f32_e32 v4, 0x3e000000, v138
	v_med3_f32 v10, v4, s58, v237
	v_mul_f32_e32 v4, 0x3e000000, v139
	v_med3_f32 v11, v4, s58, v237
	v_mov_b32_e32 v4, v199
	v_cvt_pk_fp8_f32 v4, v5, v7
	v_mov_b32_e32 v5, v199
	v_cvt_pk_fp8_f32 v5, v10, v11
	v_mul_f32_e32 v7, 0x3e000000, v140
	v_cvt_pk_fp8_f32 v4, v8, v9 op_sel:[0,0,1]
	v_mul_f32_e32 v8, 0x3e000000, v133
	v_med3_f32 v10, v8, s58, v237
	v_mul_f32_e32 v8, 0x3e000000, v134
	v_med3_f32 v9, v8, s58, v237
	v_mul_f32_e32 v8, 0x3e000000, v135
	v_med3_f32 v11, v8, s58, v237
	v_mul_f32_e32 v8, 0x3e000000, v136
	v_med3_f32 v12, v8, s58, v237
	v_mul_f32_e32 v8, 0x3e000000, v137
	v_med3_f32 v13, v8, s58, v237
	v_mul_f32_e32 v8, 0x3e000000, v130
	v_med3_f32 v14, v8, s58, v237
	v_mul_f32_e32 v8, 0x3e000000, v131
	v_med3_f32 v15, v8, s58, v237
	v_mov_b32_e32 v8, v199
	v_cvt_pk_fp8_f32 v8, v9, v11
	v_mov_b32_e32 v9, v199
	v_cvt_pk_fp8_f32 v9, v14, v15
	v_med3_f32 v7, v7, s58, v237
	v_mul_f32_e32 v11, 0x3e000000, v132
	v_cvt_pk_fp8_f32 v5, v7, v6 op_sel:[0,0,1]
	v_add_u32_e32 v6, v221, v229
	v_med3_f32 v11, v11, s58, v237
	v_ashrrev_i32_e32 v7, 31, v6
	v_cvt_pk_fp8_f32 v8, v12, v13 op_sel:[0,0,1]
	v_cvt_pk_fp8_f32 v9, v11, v10 op_sel:[0,0,1]
	v_lshlrev_b64 v[6:7], 11, v[6:7]
	v_lshl_add_u64 v[6:7], v[2:3], 0, v[6:7]
	v_mov_b32_e32 v44, v4
	v_mov_b32_e32 v45, v5
	v_mov_b32_e32 v46, v8
	v_mov_b32_e32 v47, v9
	v_lshl_add_u64 v[50:51], v[6:7], 0, v[52:53]
	s_nop 1
	v_permlane16_swap_b32_e32 v44, v46
	v_permlane16_swap_b32_e32 v45, v47
	global_store_dwordx4 v[50:51], v[44:47], off nt
	s_or_b64 exec, exec, s[4:5]
	v_cmp_lt_i32_e32 vcc, v230, v224
	s_and_saveexec_b64 s[4:5], vcc
	s_cbranch_execz .LBB0_1483
.LBB0_1491:
	v_mul_f32_e32 v4, 0x3e000000, v125
	v_med3_f32 v6, v4, s58, v237
	v_mul_f32_e32 v4, 0x3e000000, v126
	v_med3_f32 v5, v4, s58, v237
	v_mul_f32_e32 v4, 0x3e000000, v127
	v_med3_f32 v7, v4, s58, v237
	v_mul_f32_e32 v4, 0x3e000000, v128
	v_med3_f32 v8, v4, s58, v237
	v_mul_f32_e32 v4, 0x3e000000, v129
	v_med3_f32 v9, v4, s58, v237
	v_mul_f32_e32 v4, 0x3e000000, v122
	v_med3_f32 v10, v4, s58, v237
	v_mul_f32_e32 v4, 0x3e000000, v123
	v_med3_f32 v11, v4, s58, v237
	v_mov_b32_e32 v4, v199
	v_cvt_pk_fp8_f32 v4, v5, v7
	v_mov_b32_e32 v5, v199
	v_cvt_pk_fp8_f32 v5, v10, v11
	v_mul_f32_e32 v7, 0x3e000000, v124
	v_cvt_pk_fp8_f32 v4, v8, v9 op_sel:[0,0,1]
	v_mul_f32_e32 v8, 0x3e000000, v113
	v_med3_f32 v10, v8, s58, v237
	v_mul_f32_e32 v8, 0x3e000000, v118
	v_med3_f32 v9, v8, s58, v237
	v_mul_f32_e32 v8, 0x3e000000, v119
	v_med3_f32 v11, v8, s58, v237
	v_mul_f32_e32 v8, 0x3e000000, v120
	v_med3_f32 v12, v8, s58, v237
	v_mul_f32_e32 v8, 0x3e000000, v121
	v_med3_f32 v13, v8, s58, v237
	v_mul_f32_e32 v8, 0x3e000000, v110
	v_med3_f32 v14, v8, s58, v237
	v_mul_f32_e32 v8, 0x3e000000, v111
	v_med3_f32 v15, v8, s58, v237
	v_mov_b32_e32 v8, v199
	v_cvt_pk_fp8_f32 v8, v9, v11
	v_mov_b32_e32 v9, v199
	v_cvt_pk_fp8_f32 v9, v14, v15
	v_med3_f32 v7, v7, s58, v237
	v_mul_f32_e32 v11, 0x3e000000, v112
	v_cvt_pk_fp8_f32 v5, v7, v6 op_sel:[0,0,1]
	v_add_u32_e32 v6, v221, v230
	v_med3_f32 v11, v11, s58, v237
	v_ashrrev_i32_e32 v7, 31, v6
	v_cvt_pk_fp8_f32 v8, v12, v13 op_sel:[0,0,1]
	v_cvt_pk_fp8_f32 v9, v11, v10 op_sel:[0,0,1]
	v_lshlrev_b64 v[6:7], 11, v[6:7]
	v_lshl_add_u64 v[6:7], v[2:3], 0, v[6:7]
	v_mov_b32_e32 v40, v4
	v_mov_b32_e32 v41, v5
	v_mov_b32_e32 v42, v8
	v_mov_b32_e32 v43, v9
	v_lshl_add_u64 v[48:49], v[6:7], 0, v[52:53]
	s_nop 1
	v_permlane16_swap_b32_e32 v40, v42
	v_permlane16_swap_b32_e32 v41, v43
	global_store_dwordx4 v[48:49], v[40:43], off nt
	s_or_b64 exec, exec, s[4:5]
	v_cmp_lt_i32_e32 vcc, v231, v224
	s_and_saveexec_b64 s[4:5], vcc
	s_cbranch_execz .LBB0_1484
.LBB0_1492:
	v_mul_f32_e32 v4, 0x3e000000, v109
	v_med3_f32 v6, v4, s58, v237
	v_mul_f32_e32 v4, 0x3e000000, v114
	v_med3_f32 v5, v4, s58, v237
	v_mul_f32_e32 v4, 0x3e000000, v115
	v_med3_f32 v7, v4, s58, v237
	v_mul_f32_e32 v4, 0x3e000000, v116
	v_med3_f32 v8, v4, s58, v237
	v_mul_f32_e32 v4, 0x3e000000, v117
	v_med3_f32 v9, v4, s58, v237
	v_mul_f32_e32 v4, 0x3e000000, v106
	v_med3_f32 v10, v4, s58, v237
	v_mul_f32_e32 v4, 0x3e000000, v107
	v_med3_f32 v11, v4, s58, v237
	v_mov_b32_e32 v4, v199
	v_cvt_pk_fp8_f32 v4, v5, v7
	v_mov_b32_e32 v5, v199
	v_cvt_pk_fp8_f32 v5, v10, v11
	v_mul_f32_e32 v7, 0x3e000000, v108
	v_cvt_pk_fp8_f32 v4, v8, v9 op_sel:[0,0,1]
	v_mul_f32_e32 v8, 0x3e000000, v97
	v_med3_f32 v10, v8, s58, v237
	v_mul_f32_e32 v8, 0x3e000000, v102
	v_med3_f32 v9, v8, s58, v237
	v_mul_f32_e32 v8, 0x3e000000, v103
	v_med3_f32 v11, v8, s58, v237
	v_mul_f32_e32 v8, 0x3e000000, v104
	v_med3_f32 v12, v8, s58, v237
	v_mul_f32_e32 v8, 0x3e000000, v105
	v_med3_f32 v13, v8, s58, v237
	v_mul_f32_e32 v8, 0x3e000000, v94
	v_med3_f32 v14, v8, s58, v237
	v_mul_f32_e32 v8, 0x3e000000, v95
	v_med3_f32 v15, v8, s58, v237
	v_mov_b32_e32 v8, v199
	v_cvt_pk_fp8_f32 v8, v9, v11
	v_mov_b32_e32 v9, v199
	v_cvt_pk_fp8_f32 v9, v14, v15
	v_med3_f32 v7, v7, s58, v237
	v_mul_f32_e32 v11, 0x3e000000, v96
	v_cvt_pk_fp8_f32 v5, v7, v6 op_sel:[0,0,1]
	v_add_u32_e32 v6, v221, v231
	v_med3_f32 v11, v11, s58, v237
	v_ashrrev_i32_e32 v7, 31, v6
	v_cvt_pk_fp8_f32 v8, v12, v13 op_sel:[0,0,1]
	v_cvt_pk_fp8_f32 v9, v11, v10 op_sel:[0,0,1]
	v_lshlrev_b64 v[6:7], 11, v[6:7]
	v_lshl_add_u64 v[6:7], v[2:3], 0, v[6:7]
	v_mov_b32_e32 v44, v4
	v_mov_b32_e32 v45, v5
	v_mov_b32_e32 v46, v8
	v_mov_b32_e32 v47, v9
	v_lshl_add_u64 v[50:51], v[6:7], 0, v[52:53]
	s_nop 1
	v_permlane16_swap_b32_e32 v44, v46
	v_permlane16_swap_b32_e32 v45, v47
	global_store_dwordx4 v[50:51], v[44:47], off nt
	s_or_b64 exec, exec, s[4:5]
	v_cmp_lt_i32_e32 vcc, v232, v224
	s_and_saveexec_b64 s[4:5], vcc
	s_cbranch_execz .LBB0_1485
.LBB0_1493:
	v_mul_f32_e32 v4, 0x3e000000, v93
	v_med3_f32 v6, v4, s58, v237
	v_mul_f32_e32 v4, 0x3e000000, v98
	v_med3_f32 v5, v4, s58, v237
	v_mul_f32_e32 v4, 0x3e000000, v99
	v_med3_f32 v7, v4, s58, v237
	v_mul_f32_e32 v4, 0x3e000000, v100
	v_med3_f32 v8, v4, s58, v237
	v_mul_f32_e32 v4, 0x3e000000, v101
	v_med3_f32 v9, v4, s58, v237
	v_mul_f32_e32 v4, 0x3e000000, v90
	v_med3_f32 v10, v4, s58, v237
	v_mul_f32_e32 v4, 0x3e000000, v91
	v_med3_f32 v11, v4, s58, v237
	v_mov_b32_e32 v4, v199
	v_cvt_pk_fp8_f32 v4, v5, v7
	v_mov_b32_e32 v5, v199
	v_cvt_pk_fp8_f32 v5, v10, v11
	v_mul_f32_e32 v7, 0x3e000000, v92
	v_cvt_pk_fp8_f32 v4, v8, v9 op_sel:[0,0,1]
	v_mul_f32_e32 v8, 0x3e000000, v81
	v_med3_f32 v10, v8, s58, v237
	v_mul_f32_e32 v8, 0x3e000000, v86
	v_med3_f32 v9, v8, s58, v237
	v_mul_f32_e32 v8, 0x3e000000, v87
	v_med3_f32 v11, v8, s58, v237
	v_mul_f32_e32 v8, 0x3e000000, v88
	v_med3_f32 v12, v8, s58, v237
	v_mul_f32_e32 v8, 0x3e000000, v89
	v_med3_f32 v13, v8, s58, v237
	v_mul_f32_e32 v8, 0x3e000000, v78
	v_med3_f32 v14, v8, s58, v237
	v_mul_f32_e32 v8, 0x3e000000, v79
	v_med3_f32 v15, v8, s58, v237
	v_mov_b32_e32 v8, v199
	v_cvt_pk_fp8_f32 v8, v9, v11
	v_mov_b32_e32 v9, v199
	v_cvt_pk_fp8_f32 v9, v14, v15
	v_med3_f32 v7, v7, s58, v237
	v_mul_f32_e32 v11, 0x3e000000, v80
	v_cvt_pk_fp8_f32 v5, v7, v6 op_sel:[0,0,1]
	v_add_u32_e32 v6, v221, v232
	v_med3_f32 v11, v11, s58, v237
	v_ashrrev_i32_e32 v7, 31, v6
	v_cvt_pk_fp8_f32 v8, v12, v13 op_sel:[0,0,1]
	v_cvt_pk_fp8_f32 v9, v11, v10 op_sel:[0,0,1]
	v_lshlrev_b64 v[6:7], 11, v[6:7]
	v_lshl_add_u64 v[6:7], v[2:3], 0, v[6:7]
	v_mov_b32_e32 v40, v4
	v_mov_b32_e32 v41, v5
	v_mov_b32_e32 v42, v8
	v_mov_b32_e32 v43, v9
	v_lshl_add_u64 v[48:49], v[6:7], 0, v[52:53]
	s_nop 1
	v_permlane16_swap_b32_e32 v40, v42
	v_permlane16_swap_b32_e32 v41, v43
	global_store_dwordx4 v[48:49], v[40:43], off nt
	s_or_b64 exec, exec, s[4:5]
	v_cmp_lt_i32_e32 vcc, v233, v224
	s_and_saveexec_b64 s[4:5], vcc
	s_cbranch_execz .LBB0_1486
.LBB0_1494:
	v_mul_f32_e32 v4, 0x3e000000, v77
	v_med3_f32 v6, v4, s58, v237
	v_mul_f32_e32 v4, 0x3e000000, v82
	v_med3_f32 v5, v4, s58, v237
	v_mul_f32_e32 v4, 0x3e000000, v83
	v_med3_f32 v7, v4, s58, v237
	v_mul_f32_e32 v4, 0x3e000000, v84
	v_med3_f32 v8, v4, s58, v237
	v_mul_f32_e32 v4, 0x3e000000, v85
	v_med3_f32 v9, v4, s58, v237
	v_mul_f32_e32 v4, 0x3e000000, v74
	v_med3_f32 v10, v4, s58, v237
	v_mul_f32_e32 v4, 0x3e000000, v75
	v_med3_f32 v11, v4, s58, v237
	v_mov_b32_e32 v4, v199
	v_cvt_pk_fp8_f32 v4, v5, v7
	v_mov_b32_e32 v5, v199
	v_cvt_pk_fp8_f32 v5, v10, v11
	v_mul_f32_e32 v7, 0x3e000000, v76
	v_cvt_pk_fp8_f32 v4, v8, v9 op_sel:[0,0,1]
	v_mul_f32_e32 v8, 0x3e000000, v69
	v_med3_f32 v10, v8, s58, v237
	v_mul_f32_e32 v8, 0x3e000000, v70
	v_med3_f32 v9, v8, s58, v237
	v_mul_f32_e32 v8, 0x3e000000, v71
	v_med3_f32 v11, v8, s58, v237
	v_mul_f32_e32 v8, 0x3e000000, v72
	v_med3_f32 v12, v8, s58, v237
	v_mul_f32_e32 v8, 0x3e000000, v73
	v_med3_f32 v13, v8, s58, v237
	v_mul_f32_e32 v8, 0x3e000000, v66
	v_med3_f32 v14, v8, s58, v237
	v_mul_f32_e32 v8, 0x3e000000, v67
	v_med3_f32 v15, v8, s58, v237
	v_mov_b32_e32 v8, v199
	v_cvt_pk_fp8_f32 v8, v9, v11
	v_mov_b32_e32 v9, v199
	v_cvt_pk_fp8_f32 v9, v14, v15
	v_med3_f32 v7, v7, s58, v237
	v_mul_f32_e32 v11, 0x3e000000, v68
	v_cvt_pk_fp8_f32 v5, v7, v6 op_sel:[0,0,1]
	v_add_u32_e32 v6, v221, v233
	v_med3_f32 v11, v11, s58, v237
	v_ashrrev_i32_e32 v7, 31, v6
	v_cvt_pk_fp8_f32 v8, v12, v13 op_sel:[0,0,1]
	v_cvt_pk_fp8_f32 v9, v11, v10 op_sel:[0,0,1]
	v_lshlrev_b64 v[6:7], 11, v[6:7]
	v_lshl_add_u64 v[2:3], v[2:3], 0, v[6:7]
	v_mov_b32_e32 v44, v4
	v_mov_b32_e32 v45, v5
	v_mov_b32_e32 v46, v8
	v_mov_b32_e32 v47, v9
	v_lshl_add_u64 v[50:51], v[2:3], 0, v[52:53]
	s_nop 1
	v_permlane16_swap_b32_e32 v44, v46
	v_permlane16_swap_b32_e32 v45, v47
	global_store_dwordx4 v[50:51], v[44:47], off nt
	s_or_b64 exec, exec, s[4:5]
	s_and_b64 vcc, exec, s[0:1]
	s_mov_b64 s[0:1], -1
	s_cbranch_vccnz .LBB0_1466
